# w_in GEMM runs 27 column tiles (3564 tiles = 14 rounds); the 16 dt columns come from a small int8 MFMA routine at the start of the phase; plus interleaved wave index
# speedup vs baseline: 1.0087x; 1.0040x over previous
.LBB0_305:
	s_or_b64 exec, exec, s[0:1]
	v_readlane_b32 s0, v251, 5
	v_readlane_b32 s6, v251, 11
	v_readlane_b32 s7, v251, 12
	s_add_u32 s24, s6, 0x8900000
	s_addc_u32 s25, s7, 0
	v_readlane_b32 s1, v251, 6
	s_add_u32 s0, s6, 0x500000
	s_addc_u32 s1, s7, 0
	v_writelane_b32 v252, s0, 42
	v_readlane_b32 s8, v251, 28
	v_readlane_b32 s16, v251, 36
	v_writelane_b32 v252, s1, 43
	s_add_u32 s0, s6, 0x12d00000
	v_writelane_b32 v253, s0, 42
	s_addc_u32 s0, s7, 0
	v_writelane_b32 v253, s0, 43
	s_add_u32 s0, s6, 0x3cd0c0
	v_writelane_b32 v253, s0, 44
	s_addc_u32 s0, s7, 0
	v_writelane_b32 v253, s0, 45
	s_add_u32 s0, s6, 0x21800000
	v_writelane_b32 v253, s0, 46
	s_addc_u32 s0, s7, 0
	v_writelane_b32 v253, s0, 47
	s_add_u32 s0, s6, 0x3cf0c0
	v_writelane_b32 v253, s0, 48
	s_addc_u32 s0, s7, 0
	s_add_u32 s88, s6, 0x2cd0c0
	s_addc_u32 s89, s7, 0
	v_writelane_b32 v253, s0, 49
	s_add_u32 s0, s6, 0x200000
	s_addc_u32 s1, s7, 0
	v_readlane_b32 s17, v251, 37
	v_readlane_b32 s18, v251, 38
	v_readlane_b32 s19, v251, 39
	v_readlane_b32 s20, v251, 40
	v_readlane_b32 s21, v251, 41
	v_writelane_b32 v253, s0, 50
	v_readlane_b32 s22, v251, 42
	v_readlane_b32 s23, v251, 43
	s_mov_b64 s[16:17], s[20:21]
	v_writelane_b32 v253, s1, 51
	s_add_u32 s0, s16, 0x2000
	s_addc_u32 s1, s17, 0
	v_writelane_b32 v253, s0, 52
	v_readlane_b32 s4, v251, 9
	v_readlane_b32 s5, v251, 10
	v_writelane_b32 v253, s1, 53
	s_add_u32 s0, s6, 0x4ec00000
	s_addc_u32 s1, s7, 0
	v_writelane_b32 v253, s0, 54
	v_readlane_b32 s9, v251, 29
	s_mov_b64 s[4:5], s[8:9]
	v_writelane_b32 v253, s1, 55
	s_add_u32 s0, s6, 0x284000
	s_addc_u32 s1, s7, 0
	v_readlane_b32 s8, v251, 3
	v_writelane_b32 v253, s0, 56
	s_cmpk_lt_i32 s8, 0xe70
	v_readlane_b32 s10, v251, 30
	v_writelane_b32 v253, s1, 57
	s_cselect_b64 s[0:1], -1, 0
	v_writelane_b32 v253, s0, 58
	s_ashr_i32 s9, s8, 31
	v_readlane_b32 s11, v251, 31
	v_writelane_b32 v253, s1, 59
	s_lshr_b32 s0, s9, 29
	s_add_i32 s0, s8, s0
	s_ashr_i32 s10, s0, 3
	s_and_b32 s0, s0, -8
	s_sub_i32 s11, s8, s0
	s_add_u32 s0, s6, 0x58a60400
	s_addc_u32 s1, s7, 0
	v_writelane_b32 v253, s0, 60
	v_readlane_b32 s2, v251, 7
	v_readlane_b32 s3, v251, 8
	v_writelane_b32 v253, s1, 61
	s_add_u32 s0, s6, 0x5ad70400
	s_addc_u32 s1, s7, 0
	v_writelane_b32 v253, s0, 62
	v_readlane_b32 s12, v251, 32
	v_readlane_b32 s13, v251, 33
	v_writelane_b32 v253, s1, 63
	s_add_u32 s0, s6, 0x39000000
	s_addc_u32 s1, s7, 0
	v_writelane_b32 v254, s0, 0
	v_readlane_b32 s14, v251, 34
	v_readlane_b32 s15, v251, 35
	v_writelane_b32 v254, s1, 1
	s_add_u32 s0, s6, 0x4cca0400
	s_addc_u32 s1, s7, 0
	v_writelane_b32 v254, s0, 2
	s_mov_b32 s90, s57
	s_mov_b32 s65, s56
	v_writelane_b32 v254, s1, 3
	s_add_u32 s0, s6, 0x40590000
	s_addc_u32 s1, s7, 0
	s_add_u32 s72, s6, 0x4cb90000
	v_writelane_b32 v254, s0, 4
	s_addc_u32 s73, s7, 0
	s_mov_b32 s93, s56
	v_writelane_b32 v254, s1, 5
	s_add_u32 s0, s6, 0x48990000
	s_addc_u32 s1, s7, 0
	v_writelane_b32 v254, s0, 6
	v_mov_b32_e32 v67, 0
	v_mov_b32_e32 v241, 0x358637bd
	v_writelane_b32 v254, s1, 7
	s_add_u32 s0, s6, 0x5ce70400
	s_addc_u32 s1, s7, 0
	v_writelane_b32 v254, s0, 8
	v_mov_b32_e32 v188, 0x260
	v_mov_b32_e32 v189, 1
	v_writelane_b32 v254, s1, 9
	s_add_u32 s0, s6, 0x4cb98400
	v_writelane_b32 v254, s0, 10
	s_addc_u32 s0, s7, 0
	v_writelane_b32 v254, s0, 11
	s_add_u32 s0, s6, 0x58c70400
	s_addc_u32 s1, s7, 0
	v_writelane_b32 v254, s0, 12
	v_mov_b32_e32 v247, 0x3ecc95a3
	v_mbcnt_hi_u32_b32 v240, -1, v51
	v_writelane_b32 v254, s1, 13
	s_add_u32 s0, s4, 0xffc00000
	v_writelane_b32 v254, s0, 14
	s_addc_u32 s0, s5, -1
	v_writelane_b32 v254, s0, 15
	s_add_u32 s0, s6, 0x2c6000
	s_addc_u32 s1, s7, 0
	v_writelane_b32 v254, s0, 16
	v_mov_b32_e32 v0, 0x300
	v_mov_b32_e32 v250, 0x7f800000
	v_writelane_b32 v254, s1, 17
	s_add_u32 s0, s6, 0x2c7080
	s_addc_u32 s1, s7, 0
	s_add_u32 s68, s6, 0x2ee0c0
	v_writelane_b32 v254, s0, 18
	s_addc_u32 s69, s7, 0
	v_mov_b32_e32 v180, 0x3f317218
	v_writelane_b32 v254, s1, 19
	s_add_u32 s0, s6, 0x2c7084
	s_addc_u32 s1, s7, 0
	v_writelane_b32 v254, s0, 20
	v_mov_b32_e32 v182, 0x43e00000
	s_movk_i32 s91, 0x84
	v_writelane_b32 v254, s1, 21
	s_add_u32 s0, s6, 0x2c7088
	s_addc_u32 s1, s7, 0
	v_writelane_b32 v254, s0, 22
	s_movk_i32 s92, 0xc80
	s_movk_i32 s33, 0x600
	v_writelane_b32 v254, s1, 23
	s_add_u32 s0, s6, 0x2c708c
	s_addc_u32 s1, s7, 0
	v_writelane_b32 v254, s0, 24
	s_mov_b32 s94, 0xc3e00000
	s_mov_b64 s[34:35], 0x38080
	v_writelane_b32 v254, s1, 25
	s_add_u32 s0, s6, 0x2c7090
	s_addc_u32 s1, s7, 0
	v_writelane_b32 v254, s0, 26
	s_mov_b64 s[86:87], 0x58000
	s_mov_b64 s[78:79], 0x2c000
	v_writelane_b32 v254, s1, 27
	s_add_u32 s0, s6, 0x2c7094
	s_addc_u32 s1, s7, 0
	v_writelane_b32 v254, s0, 28
	s_mov_b64 s[74:75], 0x84000
	s_mov_b64 s[76:77], 0x2c080
	v_writelane_b32 v254, s1, 29
	s_add_u32 s0, s6, 0x2c7098
	s_addc_u32 s1, s7, 0
	v_writelane_b32 v254, s0, 30
	s_cmpk_lt_i32 s8, 0xb58
	s_mov_b64 s[18:19], s[22:23]
	v_writelane_b32 v254, s1, 31
	s_cselect_b64 s[0:1], -1, 0
	v_writelane_b32 v254, s0, 32
	s_cmpk_lt_i32 s8, 0x210
	s_waitcnt lgkmcnt(0)
	v_writelane_b32 v254, s1, 33
	s_cselect_b64 s[0:1], -1, 0
	v_writelane_b32 v254, s0, 34
	s_cmp_lt_i32 s11, 0
	s_barrier
	v_writelane_b32 v254, s1, 35
	s_cselect_b64 s[0:1], -1, 0
	v_writelane_b32 v254, s0, 36
	s_nop 1
	v_writelane_b32 v254, s1, 37
	s_and_b64 s[0:1], s[0:1], exec
	s_movk_i32 s0, 0x1cf
	s_cselect_b32 s0, s0, 0x1ce
	s_movk_i32 s1, 0x16c
	s_mul_i32 s0, s11, s0
	s_cselect_b32 s2, s1, 0x16b
	s_movk_i32 s1, 0x43
	s_cselect_b32 s3, s1, 0x42
	s_add_i32 s0, s0, s10
	s_mul_hi_i32 s1, s0, 0x92492493
	s_add_i32 s1, s1, s0
	s_lshr_b32 s4, s1, 31
	s_ashr_i32 s1, s1, 6
	s_add_i32 s1, s1, s4
	s_mul_i32 s4, s1, 0x70
	s_sub_i32 s0, s0, s4
	s_bfe_i32 s4, s0, 0x80000
	s_bfe_u32 s4, s4, 0x2000d
	s_add_i32 s4, s0, s4
	s_and_b32 s5, s4, 0xfc
	s_sub_i32 s0, s0, s5
	s_bfe_i32 s4, s4, 0x80000
	s_lshl_b32 s1, s1, 2
	s_sext_i32_i16 s4, s4
	s_sext_i32_i8 s0, s0
	s_add_i32 s12, s1, s0
	s_min_u32 s0, s11, 4
	s_mul_i32 s1, s11, 0x1bd
	s_add_i32 s0, s0, s1
	s_add_i32 s0, s0, s10
	s_mul_i32 s1, s0, 0x4bdb
	s_lshr_b32 s1, s1, 21
	s_mul_i32 s4, s1, 0x6c
	s_sub_i32 s4, s0, s4
	s_lshl_b32 s1, s1, 2
	s_and_b32 s0, s4, 3
	s_add_i32 s12, s1, s0
	s_ashr_i32 s0, s4, 2
	v_writelane_b32 v254, s0, 38
	s_lshr_b32 s0, s4, 2
	s_bfe_i64 s[0:1], s[0:1], 0x100000
	s_lshl_b64 s[0:1], s[0:1], 18
	v_writelane_b32 v254, s0, 39
	s_ashr_i32 s13, s12, 31
	s_nop 0
	v_writelane_b32 v254, s1, 40
	s_mov_b32 s0, s12
	v_writelane_b32 v254, s0, 41
	s_nop 1
	v_writelane_b32 v254, s1, 42
	s_lshl_b64 s[0:1], s[12:13], 18
	s_add_u32 s0, s24, s0
	s_addc_u32 s1, s25, s1
	s_add_u32 s4, s0, 0x20000
	v_writelane_b32 v254, s0, 43
	s_addc_u32 s5, s1, 0
	s_nop 0
	v_writelane_b32 v254, s1, 44
	s_mul_i32 s0, s11, s2
	s_add_i32 s0, s0, s10
	s_mul_hi_i32 s1, s0, 0x2e8ba2e9
	s_lshr_b32 s2, s1, 31
	s_ashr_i32 s1, s1, 4
	s_add_i32 s1, s1, s2
	s_mul_i32 s2, s1, 0x58
	s_sub_i32 s0, s0, s2
	s_bfe_i32 s2, s0, 0x80000
	s_bfe_u32 s2, s2, 0x2000d
	v_writelane_b32 v254, s4, 45
	s_add_i32 s2, s0, s2
	s_lshl_b32 s1, s1, 2
	v_writelane_b32 v254, s5, 46
	s_and_b32 s4, s2, 0xfc
	s_sub_i32 s0, s0, s4
	s_bfe_i32 s2, s2, 0x80000
	s_sext_i32_i16 s2, s2
	s_sext_i32_i8 s0, s0
	s_add_i32 s12, s1, s0
	s_ashr_i32 s0, s2, 2
	v_writelane_b32 v254, s0, 47
	s_lshr_b32 s0, s2, 2
	s_bfe_i64 s[0:1], s[0:1], 0x100000
	s_lshl_b64 s[0:1], s[0:1], 18
	v_writelane_b32 v254, s0, 48
	s_ashr_i32 s13, s12, 31
	v_readlane_b32 s4, v251, 2
	v_writelane_b32 v254, s1, 49
	s_mov_b32 s0, s12
	v_writelane_b32 v254, s0, 50
	s_ashr_i32 s5, s4, 31
	s_nop 0
	v_writelane_b32 v254, s1, 51
	s_lshl_b64 s[0:1], s[12:13], 18
	s_add_u32 s0, s24, s0
	v_writelane_b32 v251, s24, 24
	s_addc_u32 s1, s25, s1
	s_add_u32 s12, s0, 0x20000
	v_writelane_b32 v254, s0, 52
	s_addc_u32 s13, s1, 0
	v_writelane_b32 v251, s25, 25
	v_writelane_b32 v254, s1, 53
	s_mul_i32 s0, s11, s3
	s_add_i32 s0, s0, s10
	s_ashr_i32 s1, s0, 31
	s_lshr_b32 s1, s1, 28
	s_add_i32 s1, s0, s1
	s_and_b32 s2, s1, 0xfff0
	s_sub_i32 s0, s0, s2
	s_bfe_i32 s2, s0, 0x80000
	s_bfe_u32 s2, s2, 0x2000d
	s_add_i32 s2, s0, s2
	v_writelane_b32 v254, s12, 54
	s_and_b32 s3, s2, 0xfc
	s_sub_i32 s0, s0, s3
	v_writelane_b32 v254, s13, 55
	s_ashr_i32 s1, s1, 4
	v_writelane_b32 v254, s11, 56
	s_lshl_b32 s1, s1, 2
	s_sext_i32_i8 s0, s0
	v_writelane_b32 v254, s10, 57
	s_add_i32 s0, s1, s0
	v_writelane_b32 v254, s0, 58
	s_bfe_i32 s0, s2, 0x80000
	s_sext_i32_i16 s0, s0
	s_ashr_i32 s0, s0, 2
	v_writelane_b32 v254, s0, 59
	s_add_u32 s0, s6, 0x4cca0c00
	s_addc_u32 s1, s7, 0
	v_writelane_b32 v254, s0, 60
	v_writelane_b32 v251, s90, 18
	s_mov_b64 s[12:13], 0xa8000
	v_writelane_b32 v254, s1, 61
	s_add_u32 s0, s6, 0x4cca2c00
	s_addc_u32 s1, s7, 0
	v_writelane_b32 v254, s0, 62
	v_writelane_b32 v251, s93, 13
	s_nop 0
	v_writelane_b32 v254, s1, 63
	s_add_u32 s0, s6, 0x8900200
	v_writelane_b32 v255, s0, 0
	s_addc_u32 s0, s7, 0
	v_writelane_b32 v255, s0, 1
	s_add_u32 s0, s6, 0x500400
	v_writelane_b32 v255, s0, 2
	s_addc_u32 s0, s7, 0
	v_writelane_b32 v255, s0, 3
	s_add_u32 s0, s8, s4
	v_writelane_b32 v255, s9, 4
	v_writelane_b32 v255, s5, 5
	s_addc_u32 s1, s9, s5
	v_writelane_b32 v255, s0, 6
	s_mov_b32 s9, 0
	s_mov_b64 s[6:7], 0x38000
	v_writelane_b32 v255, s1, 7
	s_mov_b32 s0, s57
	v_writelane_b32 v255, s0, 8
	s_add_i32 s0, 0, 0x23f20
	v_writelane_b32 v255, s0, 9
	s_add_i32 s0, 0, 0x23f24
	v_writelane_b32 v255, s0, 10
	s_add_i32 s0, 0, 0x21000
	v_writelane_b32 v255, s0, 11
	s_add_i32 s0, 0, 0x21400
	v_writelane_b32 v255, s0, 12
	s_add_i32 s0, 0, 0x11c0
	v_writelane_b32 v255, s0, 13
	s_mov_b32 s1, 1
	v_writelane_b32 v255, s0, 14
	s_mov_b64 s[56:57], 0x80
	s_nop 0
	v_writelane_b32 v255, s1, 15
	v_writelane_b32 v255, s48, 16
	s_mov_b32 s0, s9
	s_nop 0
	v_writelane_b32 v255, s49, 17
	v_writelane_b32 v255, s70, 18
	s_nop 1
	v_writelane_b32 v255, s71, 19
	v_writelane_b32 v255, s80, 20
	s_nop 1
	v_writelane_b32 v255, s81, 21
	v_writelane_b32 v255, s66, 22
	s_nop 1
	v_writelane_b32 v255, s67, 23
	v_writelane_b32 v255, s84, 24
	s_nop 1
	v_writelane_b32 v255, s85, 25
	v_writelane_b32 v255, s96, 26
	s_nop 1
	v_writelane_b32 v255, s97, 27
	v_writelane_b32 v255, s65, 28
	s_branch .LBB0_309

.LBB0_453:
	s_or_b64 exec, exec, s[0:1]
	v_readlane_b32 s0, v255, 29
	v_readlane_b32 s1, v255, 30
	s_mov_b32 s1, s9
	v_readlane_b32 s36, v251, 5
	v_writelane_b32 v255, s0, 29
	v_readlane_b32 s42, v251, 11
	v_readlane_b32 s43, v251, 12
	v_writelane_b32 v255, s1, 30
	v_readlane_b32 s0, v253, 58
	s_mov_b64 s[4:5], s[42:43]
	v_readlane_b32 s8, v251, 2
	v_mov_b32_e32 v1, v246
	v_readlane_b32 s1, v253, 59
	s_waitcnt lgkmcnt(0)
	s_barrier
	v_readlane_b32 s16, v251, 21
	v_readlane_b32 s17, v251, 23
	v_readlane_b32 s18, v251, 11
	v_readlane_b32 s19, v251, 12
	v_readlane_b32 s20, v255, 29
	s_add_u32 s22, s18, 0x8900000
	s_addc_u32 s23, s19, 0
	s_mul_i32 s21, s20, 0x700000
	s_add_u32 s24, s18, s21
	s_addc_u32 s25, s19, 0
	s_add_u32 s24, s24, 0xd1c0000
	s_addc_u32 s25, s25, 0
	s_add_u32 s26, s18, 0x2cd0c0
	s_addc_u32 s27, s19, 0
	s_mul_i32 s21, s20, 0x7000
	s_add_u32 s30, s18, s21
	s_addc_u32 s31, s19, 0
	s_add_u32 s30, s30, 0x3b3cc0
	s_addc_u32 s31, s31, 0
	s_add_u32 s36, s18, 0x28801e00
	s_addc_u32 s37, s19, 0
	v_and_b32_e32 v2, 63, v246
	v_and_b32_e32 v3, 15, v2
	v_lshrrev_b32_e32 v4, 4, v2
	v_lshlrev_b32_e32 v5, 10, v3
	v_lshl_add_u32 v5, v4, 4, v5
	v_lshlrev_b32_e32 v13, 4, v4
	s_mov_b32 s38, s16
.Ldt_loop:
	s_cmpk_lt_u32 s38, 0x840
	s_cbranch_scc0 .Ldt_done
	s_lshl_b32 s39, s38, 14
	v_add_u32_e32 v6, s39, v5
	s_lshl_b32 s39, s38, 4
	v_add_u32_e32 v7, s39, v3
	v_lshlrev_b32_e32 v14, 2, v7
	s_nop 0
	global_load_dwordx4 v[84:87], v5, s[24:25] offset:0
	global_load_dwordx4 v[88:91], v5, s[24:25] offset:64
	global_load_dwordx4 v[92:95], v5, s[24:25] offset:128
	global_load_dwordx4 v[96:99], v5, s[24:25] offset:192
	global_load_dwordx4 v[100:103], v5, s[24:25] offset:256
	global_load_dwordx4 v[104:107], v5, s[24:25] offset:320
	global_load_dwordx4 v[108:111], v5, s[24:25] offset:384
	global_load_dwordx4 v[112:115], v5, s[24:25] offset:448
	global_load_dwordx4 v[132:135], v6, s[22:23] offset:0
	global_load_dwordx4 v[136:139], v6, s[22:23] offset:64
	global_load_dwordx4 v[140:143], v6, s[22:23] offset:128
	global_load_dwordx4 v[144:147], v6, s[22:23] offset:192
	global_load_dwordx4 v[148:151], v6, s[22:23] offset:256
	global_load_dwordx4 v[152:155], v6, s[22:23] offset:320
	global_load_dwordx4 v[156:159], v6, s[22:23] offset:384
	global_load_dwordx4 v[160:163], v6, s[22:23] offset:448
	global_load_dword v12, v14, s[26:27]
	global_load_dwordx4 v[16:19], v13, s[30:31]
	s_waitcnt vmcnt(0)
	v_mfma_i32_16x16x64_i8 v[8:11], v[84:87], v[132:135], 0
	v_mfma_i32_16x16x64_i8 v[8:11], v[88:91], v[136:139], v[8:11]
	v_mfma_i32_16x16x64_i8 v[8:11], v[92:95], v[140:143], v[8:11]
	v_mfma_i32_16x16x64_i8 v[8:11], v[96:99], v[144:147], v[8:11]
	v_mfma_i32_16x16x64_i8 v[8:11], v[100:103], v[148:151], v[8:11]
	v_mfma_i32_16x16x64_i8 v[8:11], v[104:107], v[152:155], v[8:11]
	v_mfma_i32_16x16x64_i8 v[8:11], v[108:111], v[156:159], v[8:11]
	v_mfma_i32_16x16x64_i8 v[8:11], v[112:115], v[160:163], v[8:11]
	s_nop 7
	global_load_dwordx4 v[84:87], v5, s[24:25] offset:512
	global_load_dwordx4 v[88:91], v5, s[24:25] offset:576
	global_load_dwordx4 v[92:95], v5, s[24:25] offset:640
	global_load_dwordx4 v[96:99], v5, s[24:25] offset:704
	global_load_dwordx4 v[100:103], v5, s[24:25] offset:768
	global_load_dwordx4 v[104:107], v5, s[24:25] offset:832
	global_load_dwordx4 v[108:111], v5, s[24:25] offset:896
	global_load_dwordx4 v[112:115], v5, s[24:25] offset:960
	global_load_dwordx4 v[132:135], v6, s[22:23] offset:512
	global_load_dwordx4 v[136:139], v6, s[22:23] offset:576
	global_load_dwordx4 v[140:143], v6, s[22:23] offset:640
	global_load_dwordx4 v[144:147], v6, s[22:23] offset:704
	global_load_dwordx4 v[148:151], v6, s[22:23] offset:768
	global_load_dwordx4 v[152:155], v6, s[22:23] offset:832
	global_load_dwordx4 v[156:159], v6, s[22:23] offset:896
	global_load_dwordx4 v[160:163], v6, s[22:23] offset:960
	s_waitcnt vmcnt(0)
	v_mfma_i32_16x16x64_i8 v[8:11], v[84:87], v[132:135], v[8:11]
	v_mfma_i32_16x16x64_i8 v[8:11], v[88:91], v[136:139], v[8:11]
	v_mfma_i32_16x16x64_i8 v[8:11], v[92:95], v[140:143], v[8:11]
	v_mfma_i32_16x16x64_i8 v[8:11], v[96:99], v[144:147], v[8:11]
	v_mfma_i32_16x16x64_i8 v[8:11], v[100:103], v[148:151], v[8:11]
	v_mfma_i32_16x16x64_i8 v[8:11], v[104:107], v[152:155], v[8:11]
	v_mfma_i32_16x16x64_i8 v[8:11], v[108:111], v[156:159], v[8:11]
	v_mfma_i32_16x16x64_i8 v[8:11], v[112:115], v[160:163], v[8:11]
	s_nop 7
	s_nop 3
	v_cvt_f32_i32_e32 v8, v8
	v_cvt_f32_i32_e32 v9, v9
	v_cvt_f32_i32_e32 v10, v10
	v_cvt_f32_i32_e32 v11, v11
	v_mul_f32_e32 v16, v12, v16
	v_mul_f32_e32 v17, v12, v17
	v_mul_f32_e32 v18, v12, v18
	v_mul_f32_e32 v19, v12, v19
	v_mul_f32_e32 v8, v8, v16
	v_mul_f32_e32 v9, v9, v17
	v_mul_f32_e32 v10, v10, v18
	v_mul_f32_e32 v11, v11, v19
	v_cvt_pk_bf16_f32 v20, v8, v9
	v_cvt_pk_bf16_f32 v21, v10, v11
	v_lshlrev_b32_e32 v22, 13, v7
	v_lshl_add_u32 v22, v4, 3, v22
	s_nop 0
	global_store_dwordx2 v22, v[20:21], s[36:37]
	s_add_i32 s38, s38, s17
	s_branch .Ldt_loop
.Ldt_done:
	s_waitcnt vmcnt(0)
	s_and_b64 vcc, exec, s[0:1]
	v_readfirstlane_b32 s36, v1
	v_readlane_b32 s37, v251, 6
	v_readlane_b32 s38, v251, 7
	v_readlane_b32 s39, v251, 8
	v_readlane_b32 s40, v251, 9
	v_readlane_b32 s41, v251, 10
	s_cbranch_vccz .LBB0_473
	v_bfe_i32 v3, v1, 27, 1
	v_lshlrev_b32_e32 v2, 4, v1
	v_lshrrev_b32_e32 v3, 22, v3
	v_add_u32_e32 v3, v2, v3
	v_and_b32_e32 v3, 0xfffffc00, v3
	v_sub_u32_e32 v2, v2, v3
	v_lshrrev_b32_e32 v3, 4, v2
	v_ashrrev_i32_e32 v5, 31, v1
	v_bitop3_b32 v2, v3, v2, 32 bitop3:0x6c
	v_lshrrev_b32_e32 v5, 26, v5
	v_readlane_b32 s16, v255, 29
	v_ashrrev_i32_e32 v3, 31, v2
	v_add_u32_e32 v5, v1, v5
	s_mul_i32 s1, s16, 0x700000
	v_lshrrev_b32_e32 v3, 26, v3
	v_ashrrev_i32_e32 v5, 6, v5
	s_mul_hi_u32 s0, s16, 0x700000
	s_add_u32 s1, s4, s1
	v_add_u32_e32 v3, v2, v3
	s_waitcnt vmcnt(14)
	v_lshlrev_b32_e32 v6, 3, v5
	s_addc_u32 s0, s5, s0
	v_ashrrev_i32_e32 v4, 6, v3
	v_and_b32_e32 v6, -16, v6
	v_and_b32_e32 v3, 0xc0, v3
	s_add_u32 s10, s1, 0xcb00000
	v_add_u32_e32 v6, v4, v6
	v_sub_u32_e32 v2, v2, v3
	s_addc_u32 s11, s0, 0
	s_ashr_i32 s37, s36, 6
	v_and_b32_e32 v4, 3, v4
	s_mov_b32 s0, 0x3fffe0
	v_lshrrev_b32_e32 v7, 2, v6
	v_lshlrev_b32_e32 v8, 1, v6
	v_lshlrev_b32_e32 v5, 5, v5
	v_ashrrev_i16_sdwa v2, v189, sext(v2) dst_sel:DWORD dst_unused:UNUSED_PAD src0_sel:DWORD src1_sel:BYTE_0
	s_ashr_i32 s44, s36, 8
	s_lshl_b32 s14, s37, 10
	v_and_or_b32 v4, v6, s0, v4
	v_and_b32_e32 v7, 4, v7
	v_and_b32_e32 v8, 24, v8
	v_and_b32_e32 v5, 32, v5
	v_bfe_i32 v2, v2, 0, 16
	v_readlane_b32 s0, v254, 39
	v_or3_b32 v4, v4, v7, v8
	v_add_lshl_u32 v2, v5, v2, 1
	v_readlane_b32 s1, v254, 40
	s_add_u32 s62, s10, s0
	v_lshl_add_u32 v148, v4, 10, v2
	s_addc_u32 s63, s11, s1
	v_mov_b32_e32 v149, v67
	s_add_i32 s15, s14, 0
	s_waitcnt vmcnt(0)
	v_lshl_add_u32 v150, v6, 10, v2
	v_lshl_add_u64 v[2:3], s[62:63], 0, v[148:149]
	s_add_i32 m0, s15, 0x10000
	s_mov_b64 s[2:3], 0x10000
	global_load_lds_dwordx4 v148, s[62:63]
	v_lshl_add_u64 v[4:5], v[2:3], 0, s[2:3]
	s_add_i32 m0, s15, 0x12000
	s_mov_b64 s[0:1], 0x20000
	global_load_lds_dwordx4 v[4:5], off
	v_lshl_add_u64 v[4:5], v[2:3], 0, s[0:1]
	s_add_i32 m0, s15, 0x14000
	s_mov_b64 s[0:1], 0x30000
	global_load_lds_dwordx4 v[4:5], off
	v_lshl_add_u64 v[4:5], v[2:3], 0, s[0:1]
	s_add_i32 m0, s15, 0x16000
	v_readlane_b32 s0, v254, 43
	global_load_lds_dwordx4 v[4:5], off
	v_mov_b32_e32 v151, v67
	v_readlane_b32 s1, v254, 44
	s_mov_b32 m0, s15
	s_add_i32 s64, s15, 0x2000
	v_lshl_add_u64 v[4:5], s[0:1], 0, v[150:151]
	v_lshl_add_u64 v[6:7], v[4:5], 0, s[2:3]
	s_add_i32 s65, s15, 0x4000
	global_load_lds_dwordx4 v150, s[0:1]
	v_readlane_b32 s0, v254, 45
	s_mov_b32 m0, s64
	v_readlane_b32 s1, v254, 46
	global_load_lds_dwordx4 v[6:7], off
	s_nop 0
	v_lshl_add_u64 v[6:7], s[0:1], 0, v[150:151]
	s_mov_b32 m0, s65
	s_add_i32 s70, s15, 0x6000
	global_load_lds_dwordx4 v150, s[0:1]
	v_lshl_add_u64 v[6:7], v[6:7], 0, s[2:3]
	s_mov_b32 m0, s70
	s_cmp_eq_u32 s44, 1
	global_load_lds_dwordx4 v[6:7], off
	s_cselect_b64 s[0:1], -1, 0
	s_cmp_lg_u32 s44, 1
	v_readlane_b32 s17, v255, 30
	s_cbranch_scc1 .LBB0_456
	s_barrier

.LBB0_459:
	s_cmp_lt_u32 s46, 0xdec
	s_cselect_b64 s[36:37], -1, 0
	s_cbranch_scc0 .LBB0_461
	s_lshr_b32 s49, s46, 3
	s_and_b32 s48, s46, 7
	s_min_u32 s51, s48, 4
	s_mul_i32 s48, s48, 0x1bd
	s_add_i32 s48, s48, s51
	s_add_i32 s48, s48, s49
	s_mul_i32 s49, s48, 0x4bdb
	s_lshr_b32 s49, s49, 21
	s_mul_i32 s51, s49, 0x6c
	s_sub_i32 s51, s48, s51
	s_lshl_b32 s50, s49, 2
	s_and_b32 s49, s51, 3
	s_add_i32 s50, s50, s49
	s_lshr_b32 s48, s51, 2
